# P5b routed stream: accumulator re-zeroing (128 v_mov after every epilogue) removed; the first stage of each pair runs a body copy whose MFMAs take SrcC=0
# speedup vs baseline: 1.0148x; 1.0060x over previous
; #define RT_UNIT(i, e, nrow, lst) do { const int lu_ = xm.lb + xm.nlb * (i); int lo_, ti_; xmap_find(xm, lu_, lo_, ti_); \
;         e = xm.x + 8 * lo_; nrow = xm.cntl[lo_] - ti_ * 256; lst = p.lists + (size_t)e * NLAT + ti_ * 256; } while (0)
; #define RT_SLOTS(lst, nrow) do { const int t_ = otid(); const int r0_ = s_row(t_, 0), r1_ = s_row(t_, 1), r2_ = s_row(t_, 2), r3_ = s_row(t_, 3); \
;         qn0 = lst[r0_ < nrow ? r0_ : 0]; qn1 = lst[r1_ < nrow ? r1_ : 0]; qn2 = lst[r2_ < nrow ? r2_ : 0]; qn3 = lst[r3_ < nrow ? r3_ : 0]; } while (0)
; #define RT_PB(e) do { const int t_ = otid(); const bf16_t* b_ = d8 + (size_t)(e) * 131072; pb0 = b_ + s_row(t_, 0) * 128 + s_ch(t_, 0); pb1 = b_ + s_row(t_, 1) * 128 + s_ch(t_, 1); } while (0)
; #define RT_A(kh) do { const int t_ = otid(); const int db_ = (kh) * 32768 + wbase, ko_ = (kh) * 64; \
;         RT_GLDS(a8 + (size_t)qn0 * 128 + s_ch(t_, 0) + ko_, db_); RT_GLDS(a8 + (size_t)qn1 * 128 + s_ch(t_, 1) + ko_, db_ + 1024); \
;         RT_GLDS(a8 + (size_t)qn2 * 128 + s_ch(t_, 2) + ko_, db_ + 2048); RT_GLDS(a8 + (size_t)qn3 * 128 + s_ch(t_, 3) + ko_, db_ + 3072); } while (0)
; #define RT_B(j) do { const int db_ = 65536 + ((j) & 1) * 32768 + wbase, ko_ = ((j) >> 1) * 32768 + ((j) & 1) * 64; \
;         RT_GLDS(pb0 + ko_, db_); RT_GLDS(pb1 + ko_, db_ + 1024); RT_GLDS(pb0 + ko_ + 2048, db_ + 2048); RT_GLDS(pb1 + ko_ + 2048, db_ + 3072); } while (0)
; __device__ void rt5b_stream(const Params& p, unsigned char* smem, const XMap& xm) {
;     ...
;             if (j & 1) asm volatile("s_waitcnt vmcnt(0)" ::: "memory");
;             asm volatile("s_waitcnt lgkmcnt(0)" ::: "memory"); __builtin_amdgcn_s_barrier(); asm volatile("" ::: "memory");
;             if (j < 7) { RT_B(j + 1); }
;             else if (have_n) { RT_A(0); RT_PB(e_n); RT_B(0); }
;             if (j == 0 && have_n) { RT_UNIT(i + 1, e_n, nrow_n, lst_n); RT_SLOTS(lst_n, nrow_n); }
;             if (wact) RT_BODY8(ldsbase + (unsigned)((j & 1) * 32768), ldsbase + 65536u + (unsigned)((j & 1) * 32768));
;             if (j & 1) {
.Lrt_bodyZ:
	s_lshl_b32 s30, s30, 15
	v_add_u32_e32 v130, s30, v249
	v_xor_b32_e32 v133, 64, v130
	s_bitset1_b32 s30, 16
	v_or_b32_e32 v135, s30, v251
	v_xor_b32_e32 v137, 64, v135
	ds_read_b128 v[184:187], v135 offset:0
	ds_read_b128 v[188:191], v137 offset:0
	ds_read_b128 v[192:195], v135 offset:0x800
	ds_read_b128 v[196:199], v137 offset:0x800
	ds_read_b128 v[200:203], v135 offset:0x1000
	ds_read_b128 v[204:207], v137 offset:0x1000
	ds_read_b128 v[208:211], v135 offset:0x1800
	ds_read_b128 v[212:215], v137 offset:0x1800
	ds_read_b128 v[216:219], v130 offset:0
	ds_read_b128 v[220:223], v133 offset:0
	ds_read_b128 v[224:227], v130 offset:0x800
	ds_read_b128 v[228:231], v133 offset:0x800
	ds_read_b128 v[232:235], v130 offset:0x1000
	ds_read_b128 v[236:239], v133 offset:0x1000
	ds_read_b128 v[240:243], v130 offset:0x1800
	ds_read_b128 v[244:247], v133 offset:0x1800
	s_waitcnt lgkmcnt(4)
	s_nop 0
	v_mfma_scale_f32_16x16x128_f8f6f4 v[126:129], v[184:191], v[216:223], 0, v179, v179 op_sel_hi:[0,0,0]
	v_mfma_scale_f32_16x16x128_f8f6f4 v[122:125], v[192:199], v[216:223], 0, v179, v179 op_sel_hi:[0,0,0]
	v_mfma_scale_f32_16x16x128_f8f6f4 v[118:121], v[200:207], v[216:223], 0, v179, v179 op_sel_hi:[0,0,0]
	v_mfma_scale_f32_16x16x128_f8f6f4 v[114:117], v[208:215], v[216:223], 0, v179, v179 op_sel_hi:[0,0,0]
	v_mfma_scale_f32_16x16x128_f8f6f4 v[110:113], v[184:191], v[224:231], 0, v179, v179 op_sel_hi:[0,0,0]
	v_mfma_scale_f32_16x16x128_f8f6f4 v[106:109], v[192:199], v[224:231], 0, v179, v179 op_sel_hi:[0,0,0]
	v_mfma_scale_f32_16x16x128_f8f6f4 v[102:105], v[200:207], v[224:231], 0, v179, v179 op_sel_hi:[0,0,0]
	v_mfma_scale_f32_16x16x128_f8f6f4 v[98:101], v[208:215], v[224:231], 0, v179, v179 op_sel_hi:[0,0,0]
	ds_read_b128 v[216:219], v130 offset:0x2000
	ds_read_b128 v[220:223], v133 offset:0x2000
	ds_read_b128 v[224:227], v130 offset:0x2800
	ds_read_b128 v[228:231], v133 offset:0x2800
	s_waitcnt lgkmcnt(4)
	v_mfma_scale_f32_16x16x128_f8f6f4 v[94:97], v[184:191], v[232:239], 0, v179, v179 op_sel_hi:[0,0,0]
	v_mfma_scale_f32_16x16x128_f8f6f4 v[90:93], v[192:199], v[232:239], 0, v179, v179 op_sel_hi:[0,0,0]
	v_mfma_scale_f32_16x16x128_f8f6f4 v[86:89], v[200:207], v[232:239], 0, v179, v179 op_sel_hi:[0,0,0]
	v_mfma_scale_f32_16x16x128_f8f6f4 v[82:85], v[208:215], v[232:239], 0, v179, v179 op_sel_hi:[0,0,0]
	v_mfma_scale_f32_16x16x128_f8f6f4 v[78:81], v[184:191], v[240:247], 0, v179, v179 op_sel_hi:[0,0,0]
	v_mfma_scale_f32_16x16x128_f8f6f4 v[74:77], v[192:199], v[240:247], 0, v179, v179 op_sel_hi:[0,0,0]
	v_mfma_scale_f32_16x16x128_f8f6f4 v[70:73], v[200:207], v[240:247], 0, v179, v179 op_sel_hi:[0,0,0]
	v_mfma_scale_f32_16x16x128_f8f6f4 v[66:69], v[208:215], v[240:247], 0, v179, v179 op_sel_hi:[0,0,0]
	ds_read_b128 v[232:235], v130 offset:0x3000
	ds_read_b128 v[236:239], v133 offset:0x3000
	ds_read_b128 v[240:243], v130 offset:0x3800
	ds_read_b128 v[244:247], v133 offset:0x3800
	s_waitcnt lgkmcnt(4)
	v_mfma_scale_f32_16x16x128_f8f6f4 v[62:65], v[184:191], v[216:223], 0, v179, v179 op_sel_hi:[0,0,0]
	v_mfma_scale_f32_16x16x128_f8f6f4 v[58:61], v[192:199], v[216:223], 0, v179, v179 op_sel_hi:[0,0,0]
	v_mfma_scale_f32_16x16x128_f8f6f4 v[54:57], v[200:207], v[216:223], 0, v179, v179 op_sel_hi:[0,0,0]
	v_mfma_scale_f32_16x16x128_f8f6f4 v[50:53], v[208:215], v[216:223], 0, v179, v179 op_sel_hi:[0,0,0]
	v_mfma_scale_f32_16x16x128_f8f6f4 v[46:49], v[184:191], v[224:231], 0, v179, v179 op_sel_hi:[0,0,0]
	v_mfma_scale_f32_16x16x128_f8f6f4 v[42:45], v[192:199], v[224:231], 0, v179, v179 op_sel_hi:[0,0,0]
	v_mfma_scale_f32_16x16x128_f8f6f4 v[38:41], v[200:207], v[224:231], 0, v179, v179 op_sel_hi:[0,0,0]
	v_mfma_scale_f32_16x16x128_f8f6f4 v[34:37], v[208:215], v[224:231], 0, v179, v179 op_sel_hi:[0,0,0]
	s_waitcnt lgkmcnt(0)
	v_mfma_scale_f32_16x16x128_f8f6f4 v[30:33], v[184:191], v[232:239], 0, v179, v179 op_sel_hi:[0,0,0]
	v_mfma_scale_f32_16x16x128_f8f6f4 v[26:29], v[192:199], v[232:239], 0, v179, v179 op_sel_hi:[0,0,0]
	v_mfma_scale_f32_16x16x128_f8f6f4 v[22:25], v[200:207], v[232:239], 0, v179, v179 op_sel_hi:[0,0,0]
	v_mfma_scale_f32_16x16x128_f8f6f4 v[18:21], v[208:215], v[232:239], 0, v179, v179 op_sel_hi:[0,0,0]
	v_mfma_scale_f32_16x16x128_f8f6f4 v[14:17], v[184:191], v[240:247], 0, v179, v179 op_sel_hi:[0,0,0]
	v_mfma_scale_f32_16x16x128_f8f6f4 v[10:13], v[192:199], v[240:247], 0, v179, v179 op_sel_hi:[0,0,0]
	v_mfma_scale_f32_16x16x128_f8f6f4 v[6:9], v[200:207], v[240:247], 0, v179, v179 op_sel_hi:[0,0,0]
	v_mfma_scale_f32_16x16x128_f8f6f4 v[2:5], v[208:215], v[240:247], 0, v179, v179 op_sel_hi:[0,0,0]
	s_branch .LBB0_1182

; __device__ void rt5b_stream(const Params& p, unsigned char* smem, const XMap& xm) {
;     ...
;         for (int j = 0; j < 8; ++j) {
;     ...
; #pragma unroll
;                 for (int m = 0; m < 8; ++m)
; #pragma unroll
;                     for (int n = 0; n < 4; ++n) acc[m][n] = (f32x4){0.f, 0.f, 0.f, 0.f};
;             }
.LBB0_1181:
.LBB0_1182:
	s_addk_i32 s76, 0x4000
	s_add_i32 s74, s74, 1
	s_addk_i32 s77, 0x80
	s_cmp_eq_u32 s74, 9
	s_cbranch_scc1 .LBB0_1162

; #define RT_UNIT(i, e, nrow, lst) do { const int lu_ = xm.lb + xm.nlb * (i); int lo_, ti_; xmap_find(xm, lu_, lo_, ti_); \
;         e = xm.x + 8 * lo_; nrow = xm.cntl[lo_] - ti_ * 256; lst = p.lists + (size_t)e * NLAT + ti_ * 256; } while (0)
; #define RT_SLOTS(lst, nrow) do { const int t_ = otid(); const int r0_ = s_row(t_, 0), r1_ = s_row(t_, 1), r2_ = s_row(t_, 2), r3_ = s_row(t_, 3); \
;         qn0 = lst[r0_ < nrow ? r0_ : 0]; qn1 = lst[r1_ < nrow ? r1_ : 0]; qn2 = lst[r2_ < nrow ? r2_ : 0]; qn3 = lst[r3_ < nrow ? r3_ : 0]; } while (0)
; #define RT_PB(e) do { const int t_ = otid(); const bf16_t* b_ = d8 + (size_t)(e) * 131072; pb0 = b_ + s_row(t_, 0) * 128 + s_ch(t_, 0); pb1 = b_ + s_row(t_, 1) * 128 + s_ch(t_, 1); } while (0)
; #define RT_A(kh) do { const int t_ = otid(); const int db_ = (kh) * 32768 + wbase, ko_ = (kh) * 64; \
;         RT_GLDS(a8 + (size_t)qn0 * 128 + s_ch(t_, 0) + ko_, db_); RT_GLDS(a8 + (size_t)qn1 * 128 + s_ch(t_, 1) + ko_, db_ + 1024); \
;         RT_GLDS(a8 + (size_t)qn2 * 128 + s_ch(t_, 2) + ko_, db_ + 2048); RT_GLDS(a8 + (size_t)qn3 * 128 + s_ch(t_, 3) + ko_, db_ + 3072); } while (0)
; #define RT_B(j) do { const int db_ = 65536 + ((j) & 1) * 32768 + wbase, ko_ = ((j) >> 1) * 32768 + ((j) & 1) * 64; \
;         RT_GLDS(pb0 + ko_, db_); RT_GLDS(pb1 + ko_, db_ + 1024); RT_GLDS(pb0 + ko_ + 2048, db_ + 2048); RT_GLDS(pb1 + ko_ + 2048, db_ + 3072); } while (0)
; __device__ void rt5b_stream(const Params& p, unsigned char* smem, const XMap& xm) {
;     ...
;             if (j & 1) asm volatile("s_waitcnt vmcnt(0)" ::: "memory");
;             asm volatile("s_waitcnt lgkmcnt(0)" ::: "memory"); __builtin_amdgcn_s_barrier(); asm volatile("" ::: "memory");
;             if (j < 7) { RT_B(j + 1); }
;             else if (have_n) { RT_A(0); RT_PB(e_n); RT_B(0); }
;             if (j == 0 && have_n) { RT_UNIT(i + 1, e_n, nrow_n, lst_n); RT_SLOTS(lst_n, nrow_n); }
;             if (wact) RT_BODY8(ldsbase + (unsigned)((j & 1) * 32768), ldsbase + 65536u + (unsigned)((j & 1) * 32768));
;             if (j & 1) {
.LBB0_1194:
	s_cmp_eq_u32 s30, 0
	s_cbranch_scc1 .Lrt_bodyZ
	s_lshl_b32 s30, s30, 15
	v_add_u32_e32 v130, s30, v249
	v_xor_b32_e32 v133, 64, v130
	s_bitset1_b32 s30, 16
	v_or_b32_e32 v135, s30, v251
	v_xor_b32_e32 v137, 64, v135
	ds_read_b128 v[184:187], v135 offset:0
	ds_read_b128 v[188:191], v137 offset:0
	ds_read_b128 v[192:195], v135 offset:0x800
	ds_read_b128 v[196:199], v137 offset:0x800
	ds_read_b128 v[200:203], v135 offset:0x1000
	ds_read_b128 v[204:207], v137 offset:0x1000
	ds_read_b128 v[208:211], v135 offset:0x1800
	ds_read_b128 v[212:215], v137 offset:0x1800
	ds_read_b128 v[216:219], v130 offset:0
	ds_read_b128 v[220:223], v133 offset:0
	ds_read_b128 v[224:227], v130 offset:0x800
	ds_read_b128 v[228:231], v133 offset:0x800
	ds_read_b128 v[232:235], v130 offset:0x1000
	ds_read_b128 v[236:239], v133 offset:0x1000
	ds_read_b128 v[240:243], v130 offset:0x1800
	ds_read_b128 v[244:247], v133 offset:0x1800
	s_waitcnt lgkmcnt(4)
	s_nop 0
	v_mfma_scale_f32_16x16x128_f8f6f4 v[126:129], v[184:191], v[216:223], v[126:129], v179, v179 op_sel_hi:[0,0,0]
	v_mfma_scale_f32_16x16x128_f8f6f4 v[122:125], v[192:199], v[216:223], v[122:125], v179, v179 op_sel_hi:[0,0,0]
	v_mfma_scale_f32_16x16x128_f8f6f4 v[118:121], v[200:207], v[216:223], v[118:121], v179, v179 op_sel_hi:[0,0,0]
	v_mfma_scale_f32_16x16x128_f8f6f4 v[114:117], v[208:215], v[216:223], v[114:117], v179, v179 op_sel_hi:[0,0,0]
	v_mfma_scale_f32_16x16x128_f8f6f4 v[110:113], v[184:191], v[224:231], v[110:113], v179, v179 op_sel_hi:[0,0,0]
	v_mfma_scale_f32_16x16x128_f8f6f4 v[106:109], v[192:199], v[224:231], v[106:109], v179, v179 op_sel_hi:[0,0,0]
	v_mfma_scale_f32_16x16x128_f8f6f4 v[102:105], v[200:207], v[224:231], v[102:105], v179, v179 op_sel_hi:[0,0,0]
	v_mfma_scale_f32_16x16x128_f8f6f4 v[98:101], v[208:215], v[224:231], v[98:101], v179, v179 op_sel_hi:[0,0,0]
	ds_read_b128 v[216:219], v130 offset:0x2000
	ds_read_b128 v[220:223], v133 offset:0x2000
	ds_read_b128 v[224:227], v130 offset:0x2800
	ds_read_b128 v[228:231], v133 offset:0x2800
	s_waitcnt lgkmcnt(4)
	v_mfma_scale_f32_16x16x128_f8f6f4 v[94:97], v[184:191], v[232:239], v[94:97], v179, v179 op_sel_hi:[0,0,0]
	v_mfma_scale_f32_16x16x128_f8f6f4 v[90:93], v[192:199], v[232:239], v[90:93], v179, v179 op_sel_hi:[0,0,0]
	v_mfma_scale_f32_16x16x128_f8f6f4 v[86:89], v[200:207], v[232:239], v[86:89], v179, v179 op_sel_hi:[0,0,0]
	v_mfma_scale_f32_16x16x128_f8f6f4 v[82:85], v[208:215], v[232:239], v[82:85], v179, v179 op_sel_hi:[0,0,0]
	v_mfma_scale_f32_16x16x128_f8f6f4 v[78:81], v[184:191], v[240:247], v[78:81], v179, v179 op_sel_hi:[0,0,0]
	v_mfma_scale_f32_16x16x128_f8f6f4 v[74:77], v[192:199], v[240:247], v[74:77], v179, v179 op_sel_hi:[0,0,0]
	v_mfma_scale_f32_16x16x128_f8f6f4 v[70:73], v[200:207], v[240:247], v[70:73], v179, v179 op_sel_hi:[0,0,0]
	v_mfma_scale_f32_16x16x128_f8f6f4 v[66:69], v[208:215], v[240:247], v[66:69], v179, v179 op_sel_hi:[0,0,0]
	ds_read_b128 v[232:235], v130 offset:0x3000
	ds_read_b128 v[236:239], v133 offset:0x3000
	ds_read_b128 v[240:243], v130 offset:0x3800
	ds_read_b128 v[244:247], v133 offset:0x3800
	s_waitcnt lgkmcnt(4)
	v_mfma_scale_f32_16x16x128_f8f6f4 v[62:65], v[184:191], v[216:223], v[62:65], v179, v179 op_sel_hi:[0,0,0]
	v_mfma_scale_f32_16x16x128_f8f6f4 v[58:61], v[192:199], v[216:223], v[58:61], v179, v179 op_sel_hi:[0,0,0]
	v_mfma_scale_f32_16x16x128_f8f6f4 v[54:57], v[200:207], v[216:223], v[54:57], v179, v179 op_sel_hi:[0,0,0]
	v_mfma_scale_f32_16x16x128_f8f6f4 v[50:53], v[208:215], v[216:223], v[50:53], v179, v179 op_sel_hi:[0,0,0]
	v_mfma_scale_f32_16x16x128_f8f6f4 v[46:49], v[184:191], v[224:231], v[46:49], v179, v179 op_sel_hi:[0,0,0]
	v_mfma_scale_f32_16x16x128_f8f6f4 v[42:45], v[192:199], v[224:231], v[42:45], v179, v179 op_sel_hi:[0,0,0]
	v_mfma_scale_f32_16x16x128_f8f6f4 v[38:41], v[200:207], v[224:231], v[38:41], v179, v179 op_sel_hi:[0,0,0]
	v_mfma_scale_f32_16x16x128_f8f6f4 v[34:37], v[208:215], v[224:231], v[34:37], v179, v179 op_sel_hi:[0,0,0]
	s_waitcnt lgkmcnt(0)
	v_mfma_scale_f32_16x16x128_f8f6f4 v[30:33], v[184:191], v[232:239], v[30:33], v179, v179 op_sel_hi:[0,0,0]
	v_mfma_scale_f32_16x16x128_f8f6f4 v[26:29], v[192:199], v[232:239], v[26:29], v179, v179 op_sel_hi:[0,0,0]
	v_mfma_scale_f32_16x16x128_f8f6f4 v[22:25], v[200:207], v[232:239], v[22:25], v179, v179 op_sel_hi:[0,0,0]
	v_mfma_scale_f32_16x16x128_f8f6f4 v[18:21], v[208:215], v[232:239], v[18:21], v179, v179 op_sel_hi:[0,0,0]
	v_mfma_scale_f32_16x16x128_f8f6f4 v[14:17], v[184:191], v[240:247], v[14:17], v179, v179 op_sel_hi:[0,0,0]
	v_mfma_scale_f32_16x16x128_f8f6f4 v[10:13], v[192:199], v[240:247], v[10:13], v179, v179 op_sel_hi:[0,0,0]
	v_mfma_scale_f32_16x16x128_f8f6f4 v[6:9], v[200:207], v[240:247], v[6:9], v179, v179 op_sel_hi:[0,0,0]
	v_mfma_scale_f32_16x16x128_f8f6f4 v[2:5], v[208:215], v[240:247], v[2:5], v179, v179 op_sel_hi:[0,0,0]
	s_andn2_b64 vcc, exec, s[58:59]
	s_cbranch_vccnz .LBB0_1182
